# prep: weight-folding waves run at s_setprio 3 (they share CUs with the streaming conversion waves)
# baseline (speedup 1.0000x reference)
.LBB0_3:
	s_setprio 3
	s_load_dwordx2 s[4:5], s[0:1], 0x0
	s_load_dwordx2 s[6:7], s[0:1], 0x10
	s_add_i32 s3, s2, 0xffffff00
	s_cmp_gt_i32 s3, 63
	s_mov_b64 s[8:9], -1
	s_cbranch_scc0 .LBB0_34
	s_cmpk_gt_u32 s3, 0x7f
	s_cbranch_scc0 .LBB0_29
	s_load_dwordx2 s[12:13], s[0:1], 0x8
	s_load_dwordx2 s[14:15], s[0:1], 0x18
	s_cmpk_gt_u32 s3, 0x87
	s_cbranch_scc0 .LBB0_25
	v_lshlrev_b32_e32 v1, 2, v0
	s_waitcnt lgkmcnt(0)
	global_load_dword v2, v1, s[12:13]
	global_load_dword v3, v1, s[14:15]
	s_movk_i32 s8, 0x80
	v_cmp_gt_u32_e32 vcc, s8, v0
	s_waitcnt vmcnt(0)
	v_mul_f32_e32 v2, v2, v3
	ds_write_b32 v1, v2
	s_waitcnt lgkmcnt(0)
	s_barrier
	s_and_saveexec_b64 s[8:9], vcc
	s_cbranch_execz .LBB0_8
	ds_read2st64_b32 v[2:3], v1 offset1:2
	s_waitcnt lgkmcnt(0)
	v_add_f32_e32 v2, v3, v2
	ds_write_b32 v1, v2
